# helper-wave L2 warm-up: idle waves 13-15 stream the block's h1s slice into L2 after the grid barrier
# speedup vs baseline: 1.0143x; 1.0143x over previous
.LBB2_350:
	v_readfirstlane_b32 s91, v0
	v_and_b32_e32 v1, 0x3c0, v0
	s_lshr_b32 s91, s91, 6
	s_cmp_ge_u32 s91, 13
	s_cbranch_scc1 .Lhelper_pf
	s_movk_i32 s0, 0x31f
	v_cmp_gt_u32_e32 vcc, s0, v1
	s_and_saveexec_b64 s[0:1], vcc
	s_cbranch_execz .LBB2_371
	s_andn2_b64 vcc, exec, s[4:5]
	s_cbranch_vccnz .LBB2_365
	v_add_u32_e32 v1, 8, v46
	v_mov_b32_e32 v43, 0x3f80
	v_mov_b32_e32 v42, 1.0
	v_cmp_le_u32_e32 vcc, v1, v47
	v_mov_b32_e32 v7, 0
	v_mov_b32_e32 v6, 0
	v_mov_b32_e32 v9, 0
	v_mov_b32_e32 v8, 0
	v_mov_b32_e32 v3, 0
	v_mov_b32_e32 v2, 0
	v_mov_b32_e32 v5, 0
	v_mov_b32_e32 v4, 0
	s_and_saveexec_b64 s[0:1], vcc
	s_cbranch_execz .LBB2_356
	v_mov_b32_e32 v1, v44
	v_lshlrev_b32_e32 v45, 2, v46
	v_mov_b32_e32 v5, 0
	s_mov_b64 s[2:3], 0
	v_mov_b32_e32 v4, 0
	v_mov_b32_e32 v3, 0
	v_mov_b32_e32 v2, 0
	v_mov_b32_e32 v9, 0
	v_mov_b32_e32 v8, 0
	v_mov_b32_e32 v7, 0
	v_mov_b32_e32 v6, 0

.Lhelper_pf:
	s_sub_i32 s84, s91, 13
	s_lshl_b32 s84, s84, 6
	s_lshl_b32 s85, s83, 10
	s_add_i32 s84, s84, s85
	v_and_b32_e32 v2, 63, v0
	v_add_u32_e32 v2, s84, v2
	v_mov_b32_e32 v3, v2
	v_min_u32_e32 v3, 0x61a7, v3
	v_lshlrev_b32_e32 v3, 7, v3
	global_load_dword v10, v3, s[62:63]
	v_add_u32_e32 v3, 192, v2
	v_min_u32_e32 v3, 0x61a7, v3
	v_lshlrev_b32_e32 v3, 7, v3
	global_load_dword v11, v3, s[62:63]
	v_add_u32_e32 v3, 384, v2
	v_min_u32_e32 v3, 0x61a7, v3
	v_lshlrev_b32_e32 v3, 7, v3
	global_load_dword v12, v3, s[62:63]
	v_add_u32_e32 v3, 576, v2
	v_min_u32_e32 v3, 0x61a7, v3
	v_lshlrev_b32_e32 v3, 7, v3
	global_load_dword v13, v3, s[62:63]
	v_add_u32_e32 v3, 768, v2
	v_min_u32_e32 v3, 0x61a7, v3
	v_lshlrev_b32_e32 v3, 7, v3
	global_load_dword v14, v3, s[62:63]
	v_add_u32_e32 v3, 960, v2
	v_min_u32_e32 v3, 0x61a7, v3
	v_lshlrev_b32_e32 v3, 7, v3
	global_load_dword v15, v3, s[62:63]
	s_waitcnt vmcnt(0)
	s_endpgm
